# baseline (speedup 1.0000x reference)
.Lattn_g_done:
	s_and_saveexec_b64 s[40:41], s[0:1]
	s_cbranch_execz .LBB0_108
	v_mov_b32_e32 v2, v54
	s_waitcnt vmcnt(5)
	v_mov_b32_e32 v99, v112
	v_permlane16_swap_b32_e32 v2, v54
	v_mov_b32_e32 v100, v113
	v_mov_b32_e32 v101, v114
	v_add_f32_e32 v54, v54, v2
	v_mov_b32_e32 v55, v54
	v_mov_b32_e32 v102, v115
	s_nop 0
	v_permlane32_swap_b32_e32 v55, v54
	s_lshl_b32 s95, s80, 1
	v_mov_b32_e32 v2, s95
	v_or_b32_e32 v4, 1, v2
	v_cmp_gt_i32_e32 vcc, s33, v4
	ds_read_b128 v[4:7], v86 offset:32768
	ds_read_b128 v[8:11], v86 offset:33792
	ds_read_b128 v[12:15], v86 offset:34816
	ds_read_b128 v[16:19], v86 offset:35840
	ds_read_b128 v[104:107], v86 offset:40960
	ds_read_b128 v[108:111], v86 offset:41984
	ds_read_b128 v[112:115], v86 offset:43008
	ds_read_b128 v[116:119], v86 offset:44032
	v_cvt_pk_f16_f32 v53, v52, v53
	v_cvt_pk_f16_f32 v52, v50, v51
	v_cvt_pk_f16_f32 v51, v48, v49
	v_cvt_pk_f16_f32 v50, v46, v47
	v_cvt_pk_f16_f32 v45, v44, v45
	v_cvt_pk_f16_f32 v44, v42, v43
	v_cvt_pk_f16_f32 v43, v40, v41
	v_cvt_pk_f16_f32 v42, v38, v39
	v_cvt_pk_f16_f32 v37, v36, v37
	v_cvt_pk_f16_f32 v36, v34, v35
	v_cvt_pk_f16_f32 v35, v32, v33
	v_cvt_pk_f16_f32 v34, v30, v31
	v_cvt_pk_f16_f32 v63, v28, v29
	v_cvt_pk_f16_f32 v62, v26, v27
	v_cvt_pk_f16_f32 v61, v24, v25
	v_cvt_pk_f16_f32 v60, v22, v23
	ds_read_b128 v[20:23], v86 offset:36864
	ds_read_b128 v[24:27], v86 offset:37888
	ds_read_b128 v[28:31], v86 offset:38912
	ds_read_b128 v[38:41], v86 offset:39936
	s_waitcnt lgkmcnt(8)
	v_mfma_f32_16x16x32_f16 v[46:49], v[4:7], v[50:53], 0
	v_mfma_f32_16x16x32_f16 v[46:49], v[8:11], v[42:45], v[46:49]
	v_mfma_f32_16x16x32_f16 v[46:49], v[12:15], v[34:37], v[46:49]
	v_mfma_f32_16x16x32_f16 v[46:49], v[16:19], v[60:63], v[46:49]
	ds_read_b128 v[4:7], v86 offset:45056
	ds_read_b128 v[8:11], v86 offset:46080
	ds_read_b128 v[12:15], v86 offset:47104
	ds_read_b128 v[16:19], v86 offset:48128
	s_waitcnt lgkmcnt(4)
	v_mfma_f32_16x16x32_f16 v[56:59], v[20:23], v[50:53], 0
	v_mfma_f32_16x16x32_f16 v[56:59], v[24:27], v[42:45], v[56:59]
	v_mfma_f32_16x16x32_f16 v[56:59], v[28:31], v[34:37], v[56:59]
	v_mfma_f32_16x16x32_f16 v[56:59], v[38:41], v[60:63], v[56:59]
	ds_read_b128 v[20:23], v86 offset:49152
	ds_read_b128 v[24:27], v86 offset:50176
	ds_read_b128 v[28:31], v86 offset:51200
	ds_read_b128 v[38:41], v86 offset:52224
	v_cndmask_b32_e64 v64, 0, v46, s[14:15]
	v_cndmask_b32_e64 v65, 0, v47, s[14:15]
	v_cndmask_b32_e64 v66, 0, v48, s[14:15]
	v_cndmask_b32_e64 v67, 0, v49, s[14:15]
	v_mfma_f32_16x16x32_f16 v[46:49], v[104:107], v[50:53], 0
	v_mfma_f32_16x16x32_f16 v[46:49], v[108:111], v[42:45], v[46:49]
	v_mfma_f32_16x16x32_f16 v[46:49], v[112:115], v[34:37], v[46:49]
	v_mfma_f32_16x16x32_f16 v[46:49], v[116:119], v[60:63], v[46:49]
	ds_read_b128 v[104:107], v86 offset:53248
	ds_read_b128 v[108:111], v86 offset:54272
	ds_read_b128 v[112:115], v86 offset:55296
	ds_read_b128 v[116:119], v86 offset:56320
	v_cndmask_b32_e64 v64, v64, v56, s[12:13]
	v_cndmask_b32_e64 v65, v65, v57, s[12:13]
	v_cndmask_b32_e64 v66, v66, v58, s[12:13]
	v_cndmask_b32_e64 v67, v67, v59, s[12:13]
	s_waitcnt lgkmcnt(8)
	v_mfma_f32_16x16x32_f16 v[56:59], v[4:7], v[50:53], 0
	v_mfma_f32_16x16x32_f16 v[56:59], v[8:11], v[42:45], v[56:59]
	v_mfma_f32_16x16x32_f16 v[56:59], v[12:15], v[34:37], v[56:59]
	v_mfma_f32_16x16x32_f16 v[56:59], v[16:19], v[60:63], v[56:59]
	ds_read_b128 v[4:7], v86 offset:57344
	ds_read_b128 v[8:11], v86 offset:58368
	ds_read_b128 v[12:15], v86 offset:59392
	ds_read_b128 v[16:19], v86 offset:60416
	v_cndmask_b32_e64 v64, v64, v46, s[10:11]
	v_cndmask_b32_e64 v65, v65, v47, s[10:11]
	v_cndmask_b32_e64 v66, v66, v48, s[10:11]
	v_cndmask_b32_e64 v67, v67, v49, s[10:11]
	s_waitcnt lgkmcnt(8)
	v_mfma_f32_16x16x32_f16 v[46:49], v[20:23], v[50:53], 0
	v_mfma_f32_16x16x32_f16 v[46:49], v[24:27], v[42:45], v[46:49]
	v_mfma_f32_16x16x32_f16 v[46:49], v[28:31], v[34:37], v[46:49]
	v_mfma_f32_16x16x32_f16 v[46:49], v[38:41], v[60:63], v[46:49]
	ds_read_b128 v[20:23], v86 offset:61440
	ds_read_b128 v[24:27], v86 offset:62464
	ds_read_b128 v[28:31], v86 offset:63488
	ds_read_b128 v[38:41], v86 offset:64512
	v_cndmask_b32_e64 v64, v64, v56, s[8:9]
	v_cndmask_b32_e64 v65, v65, v57, s[8:9]
	v_cndmask_b32_e64 v66, v66, v58, s[8:9]
	v_cndmask_b32_e64 v67, v67, v59, s[8:9]
	s_waitcnt lgkmcnt(8)
	v_mfma_f32_16x16x32_f16 v[56:59], v[104:107], v[50:53], 0
	v_mfma_f32_16x16x32_f16 v[56:59], v[108:111], v[42:45], v[56:59]
	v_mfma_f32_16x16x32_f16 v[56:59], v[112:115], v[34:37], v[56:59]
	v_mfma_f32_16x16x32_f16 v[56:59], v[116:119], v[60:63], v[56:59]
	s_nop 3
	v_cndmask_b32_e64 v64, v64, v46, s[6:7]
	v_cndmask_b32_e64 v65, v65, v47, s[6:7]
	v_cndmask_b32_e64 v66, v66, v48, s[6:7]
	v_cndmask_b32_e64 v67, v67, v49, s[6:7]
	s_waitcnt lgkmcnt(4)
	v_mfma_f32_16x16x32_f16 v[46:49], v[4:7], v[50:53], 0
	v_mfma_f32_16x16x32_f16 v[46:49], v[8:11], v[42:45], v[46:49]
	v_mfma_f32_16x16x32_f16 v[46:49], v[12:15], v[34:37], v[46:49]
	v_mfma_f32_16x16x32_f16 v[46:49], v[16:19], v[60:63], v[46:49]
	s_nop 3
	v_cndmask_b32_e64 v64, v64, v56, s[20:21]
	v_cndmask_b32_e64 v65, v65, v57, s[20:21]
	v_cndmask_b32_e64 v66, v66, v58, s[20:21]
	v_cndmask_b32_e64 v67, v67, v59, s[20:21]
	s_waitcnt lgkmcnt(0)
	v_mfma_f32_16x16x32_f16 v[56:59], v[20:23], v[50:53], 0
	v_mfma_f32_16x16x32_f16 v[56:59], v[24:27], v[42:45], v[56:59]
	v_mfma_f32_16x16x32_f16 v[56:59], v[28:31], v[34:37], v[56:59]
	v_mfma_f32_16x16x32_f16 v[56:59], v[38:41], v[60:63], v[56:59]
	s_nop 3
	v_cndmask_b32_e64 v64, v64, v46, s[18:19]
	v_cndmask_b32_e64 v65, v65, v47, s[18:19]
	v_cndmask_b32_e64 v66, v66, v48, s[18:19]
	v_cndmask_b32_e64 v67, v67, v49, s[18:19]
	s_nop 7
	v_cndmask_b32_e64 v64, v64, v56, s[16:17]
	v_cndmask_b32_e64 v65, v65, v57, s[16:17]
	v_cndmask_b32_e64 v66, v66, v58, s[16:17]
	v_cndmask_b32_e64 v67, v67, v59, s[16:17]
	s_or_b64 s[42:43], s[38:39], vcc
	s_and_saveexec_b64 s[0:1], s[42:43]
	s_cbranch_execz .LBB0_105
	v_add_f32_e32 v40, v54, v55
	v_lshlrev_b32_e32 v36, 1, v78
	v_cmp_lt_f32_e32 vcc, 0, v40
	v_rcp_f32_e32 v12, v40
	ds_read_b128 v[36:39], v36 offset:27472
	v_or_b32_e32 v2, v2, v89
	v_cndmask_b32_e32 v8, 0, v12, vcc
	s_waitcnt lgkmcnt(0)
	v_fma_mixlo_f16 v4, v8, v64, v36
	v_fma_mixlo_f16 v5, v8, v65, v37
	v_fma_mixlo_f16 v6, v8, v66, v38
	v_fma_mixlo_f16 v7, v8, v67, v39
	v_cndmask_b32_e32 v4, 0, v4, vcc
	v_cndmask_b32_e32 v8, 0, v5, vcc
	v_cndmask_b32_e32 v5, 0, v6, vcc
	v_cndmask_b32_e32 v6, 0, v7, vcc
	v_pack_b32_f16 v5, v5, v6
	v_pack_b32_f16 v4, v4, v8
	v_mad_u64_u32 v[6:7], s[42:43], v2, s72, v[78:79]
	ds_write_b64 v6, v[4:5]
